# ph10 prefix loads batched in one round trip; ph14 count table read with normal cache policy; ph3 second-half parameter loads issued with the first batch
# baseline (speedup 1.0000x reference)
.LBB0_473:
	v_lshl_add_u32 v214, s62, 8, v169
	v_lshl_or_b32 v106, s63, 7, v221
	v_add_u32_e32 v190, 0xa0, v214
	v_ashrrev_i32_e32 v107, 31, v106
	v_add_u32_e32 v198, 0x80, v214
	v_add_u32_e32 v210, 16, v214
	v_add_u32_e32 v206, 32, v214
	v_add_u32_e32 v204, 48, v214
	v_add_u32_e32 v194, 0x90, v214
	v_ashrrev_i32_e32 v191, 31, v190
	v_add_u32_e32 v180, 0xb0, v214
	v_lshl_add_u64 v[108:109], v[106:107], 1, s[26:27]
	v_ashrrev_i32_e32 v199, 31, v198
	v_ashrrev_i32_e32 v215, 31, v214
	v_ashrrev_i32_e32 v211, 31, v210
	v_ashrrev_i32_e32 v207, 31, v206
	v_ashrrev_i32_e32 v205, 31, v204
	v_ashrrev_i32_e32 v195, 31, v194
	v_lshlrev_b64 v[156:157], 11, v[190:191]
	v_ashrrev_i32_e32 v181, 31, v180
	v_lshlrev_b64 v[110:111], 11, v[198:199]
	v_lshlrev_b64 v[112:113], 11, v[214:215]
	v_lshlrev_b64 v[114:115], 11, v[210:211]
	v_lshlrev_b64 v[116:117], 11, v[206:207]
	v_lshlrev_b64 v[152:153], 11, v[204:205]
	v_lshlrev_b64 v[154:155], 11, v[194:195]
	v_lshl_add_u64 v[170:171], v[108:109], 0, v[156:157]
	v_lshlrev_b64 v[156:157], 11, v[180:181]
	v_lshlrev_b64 v[186:187], 2, v[106:107]
	v_lshl_add_u64 v[112:113], v[108:109], 0, v[112:113]
	v_lshl_add_u64 v[114:115], v[108:109], 0, v[114:115]
	v_lshl_add_u64 v[116:117], v[108:109], 0, v[116:117]
	v_lshl_add_u64 v[152:153], v[108:109], 0, v[152:153]
	v_lshl_add_u64 v[110:111], v[108:109], 0, v[110:111]
	v_lshl_add_u64 v[154:155], v[108:109], 0, v[154:155]
	v_lshl_add_u64 v[108:109], v[108:109], 0, v[156:157]
	v_lshl_add_u64 v[182:183], s[30:31], 0, v[186:187]
	flat_load_dwordx2 v[218:219], v[112:113]
	flat_load_dwordx2 v[216:217], v[114:115]
	flat_load_dwordx2 v[212:213], v[116:117]
	flat_load_dwordx2 v[202:203], v[110:111]
	flat_load_dwordx2 v[208:209], v[152:153]
	flat_load_dwordx2 v[200:201], v[154:155]
	flat_load_dwordx2 v[196:197], v[170:171]
	flat_load_dwordx2 v[192:193], v[108:109]
	flat_load_dwordx2 v[178:179], v[112:113] offset:32
	flat_load_dwordx2 v[164:165], v[114:115] offset:32
	flat_load_dwordx2 v[162:163], v[116:117] offset:32
	flat_load_dwordx2 v[160:161], v[152:153] offset:32
	flat_load_dwordx2 v[158:159], v[110:111] offset:32
	flat_load_dwordx2 v[156:157], v[154:155] offset:32
	s_nop 0
	flat_load_dwordx2 v[154:155], v[170:171] offset:32
	flat_load_dwordx2 v[152:153], v[108:109] offset:32
	flat_load_dwordx4 v[114:117], v[182:183]
	v_lshl_add_u64 v[188:189], s[36:37], 0, v[186:187]
	v_lshl_add_u64 v[184:185], s[34:35], 0, v[186:187]
	flat_load_dwordx4 v[110:113], v[188:189]
	flat_load_dwordx4 v[106:109], v[184:185]
	flat_load_dwordx4 v[234:237], v[182:183] offset:64
	flat_load_dwordx4 v[238:241], v[184:185] offset:64
	flat_load_dwordx4 v[242:245], v[188:189] offset:64
	s_mov_b64 s[62:63], -1
	s_andn2_b64 vcc, exec, s[54:55]
	s_waitcnt vmcnt(0) lgkmcnt(0)
	v_lshlrev_b32_e32 v170, 16, v218
	v_and_b32_e32 v171, 0xffff0000, v218
	v_lshlrev_b32_e32 v223, 16, v219
	v_and_b32_e32 v218, 0xffff0000, v219
	v_add_f32_e32 v138, v138, v114
	v_mul_f32_e32 v138, 0xbfb8aa3b, v138
	v_exp_f32_e32 v138, v138
	v_add_f32_e32 v130, v130, v114
	v_add_f32_e32 v134, v134, v106
	v_mul_f32_e32 v134, 0xbfb8aa3b, v134
	v_add_f32_e32 v138, 1.0, v138
	v_rcp_f32_e32 v138, v138
	v_exp_f32_e32 v134, v134
	v_add_f32_e32 v135, v135, v107
	v_mul_f32_e32 v135, 0xbfb8aa3b, v135
	v_mul_f32_e64 v138, v138, -v110
	v_add_f32_e32 v172, v138, v138
	v_exp_f32_e32 v172, v172
	v_add_f32_e32 v134, 1.0, v134
	v_rcp_f32_e32 v134, v134
	v_exp_f32_e32 v135, v135
	v_sub_f32_e32 v172, 1.0, v172
	v_max_f32_e32 v172, 0, v172
	v_sqrt_f32_e32 v172, v172
	v_add_f32_e32 v135, 1.0, v135
	v_rcp_f32_e32 v135, v135
	v_add_f32_e32 v136, v136, v108
	v_mul_f32_e32 v134, v134, v172
	v_mul_f32_e32 v134, v134, v170
	v_cvt_pk_bf16_f32 v134, v134, v138
	v_add_f32_e32 v138, v139, v115
	v_mul_f32_e32 v138, 0xbfb8aa3b, v138
	v_exp_f32_e32 v138, v138
	v_mul_f32_e32 v136, 0xbfb8aa3b, v136
	v_exp_f32_e32 v136, v136
	v_mul_f32_e32 v130, 0xbfb8aa3b, v130
	v_add_f32_e32 v138, 1.0, v138
	v_rcp_f32_e32 v138, v138
	v_add_f32_e32 v136, 1.0, v136
	v_rcp_f32_e32 v136, v136
	v_exp_f32_e32 v130, v130
	v_mul_f32_e64 v138, v138, -v111
	v_add_f32_e32 v139, v138, v138
	v_exp_f32_e32 v139, v139
	v_add_f32_e32 v130, 1.0, v130
	v_add_f32_e32 v137, v137, v109
	v_rcp_f32_e32 v130, v130
	v_sub_f32_e32 v139, 1.0, v139
	v_max_f32_e32 v139, 0, v139
	v_sqrt_f32_e32 v139, v139
	v_mul_f32_e32 v137, 0xbfb8aa3b, v137
	v_exp_f32_e32 v137, v137
	v_mul_f32_e64 v130, v130, -v110
	v_mul_f32_e32 v135, v135, v139
	v_mul_f32_e32 v135, v135, v171
	v_cvt_pk_bf16_f32 v135, v135, v138
	v_add_f32_e32 v138, v140, v116
	v_mul_f32_e32 v138, 0xbfb8aa3b, v138
	v_exp_f32_e32 v138, v138
	v_add_f32_e32 v126, v126, v106
	v_add_f32_e32 v140, v130, v130
	v_add_f32_e32 v137, 1.0, v137
	v_add_f32_e32 v138, 1.0, v138
	v_rcp_f32_e32 v138, v138
	v_mul_f32_e32 v126, 0xbfb8aa3b, v126
	v_exp_f32_e32 v140, v140
	v_rcp_f32_e32 v137, v137
	v_mul_f32_e64 v138, v138, -v112
	v_add_f32_e32 v139, v138, v138
	v_exp_f32_e32 v139, v139
	v_exp_f32_e32 v126, v126
	v_sub_f32_e32 v140, 1.0, v140
	v_max_f32_e32 v140, 0, v140
	v_sub_f32_e32 v139, 1.0, v139
	v_max_f32_e32 v139, 0, v139
	v_sqrt_f32_e32 v139, v139
	v_add_f32_e32 v126, 1.0, v126
	v_rcp_f32_e32 v126, v126
	v_sqrt_f32_e32 v140, v140
	v_mul_f32_e32 v136, v136, v139
	v_mul_f32_e32 v136, v136, v223
	v_cvt_pk_bf16_f32 v136, v136, v138
	v_add_f32_e32 v138, v141, v117
	v_mul_f32_e32 v138, 0xbfb8aa3b, v138
	v_exp_f32_e32 v138, v138
	v_mul_f32_e32 v126, v126, v140
	v_add_f32_e32 v127, v127, v107
	v_mul_f32_e32 v127, 0xbfb8aa3b, v127
	v_add_f32_e32 v138, 1.0, v138
	v_rcp_f32_e32 v138, v138
	v_exp_f32_e32 v127, v127
	v_add_f32_e32 v122, v122, v114
	v_mul_f32_e32 v122, 0xbfb8aa3b, v122
	v_mul_f32_e64 v138, v138, -v113
	v_add_f32_e32 v139, v138, v138
	v_exp_f32_e32 v139, v139
	v_add_f32_e32 v127, 1.0, v127
	v_rcp_f32_e32 v127, v127
	v_exp_f32_e32 v122, v122
	v_sub_f32_e32 v139, 1.0, v139
	v_max_f32_e32 v139, 0, v139
	v_sqrt_f32_e32 v139, v139
	v_add_f32_e32 v122, 1.0, v122
	v_rcp_f32_e32 v122, v122
	v_add_f32_e32 v118, v118, v106
	v_mul_f32_e32 v137, v137, v139
	v_mul_f32_e32 v137, v137, v218
	v_cvt_pk_bf16_f32 v137, v137, v138
	v_lshlrev_b64 v[138:139], 12, v[214:215]
	v_lshl_add_u64 v[138:139], s[38:39], 0, v[138:139]
	v_lshl_add_u64 v[138:139], v[138:139], 0, v[186:187]
	flat_store_dwordx4 v[138:139], v[134:137]
	v_mul_f32_e64 v122, v122, -v110
	v_mul_f32_e32 v118, 0xbfb8aa3b, v118
	v_lshlrev_b32_e32 v134, 16, v216
	v_mul_f32_e32 v126, v126, v134
	v_cvt_pk_bf16_f32 v130, v126, v130
	v_add_f32_e32 v126, v131, v115
	v_mul_f32_e32 v126, 0xbfb8aa3b, v126
	v_exp_f32_e32 v126, v126
	v_and_b32_e32 v135, 0xffff0000, v216
	v_lshlrev_b32_e32 v136, 16, v217
	v_and_b32_e32 v137, 0xffff0000, v217
	v_add_f32_e32 v126, 1.0, v126
	v_rcp_f32_e32 v126, v126
	v_exp_f32_e32 v118, v118
	v_add_f32_e32 v119, v119, v107
	v_mul_f32_e32 v119, 0xbfb8aa3b, v119
	v_mul_f32_e64 v126, v126, -v111
	v_add_f32_e32 v131, v126, v126
	v_exp_f32_e32 v131, v131
	v_add_f32_e32 v118, 1.0, v118
	v_rcp_f32_e32 v118, v118
	v_exp_f32_e32 v119, v119
	v_sub_f32_e32 v131, 1.0, v131
	v_max_f32_e32 v131, 0, v131
	v_sqrt_f32_e32 v131, v131
	v_add_f32_e32 v119, 1.0, v119
	v_rcp_f32_e32 v119, v119
	v_add_f32_e32 v102, v102, v114
	v_mul_f32_e32 v127, v127, v131
	v_mul_f32_e32 v127, v127, v135
	v_cvt_pk_bf16_f32 v131, v127, v126
	v_add_f32_e32 v126, v132, v116
	v_mul_f32_e32 v126, 0xbfb8aa3b, v126
	v_exp_f32_e32 v126, v126
	v_add_f32_e32 v127, v128, v108
	v_mul_f32_e32 v127, 0xbfb8aa3b, v127
	v_exp_f32_e32 v127, v127
	v_add_f32_e32 v126, 1.0, v126
	v_rcp_f32_e32 v126, v126
	v_mul_f32_e32 v102, 0xbfb8aa3b, v102
	v_add_f32_e32 v127, 1.0, v127
	v_rcp_f32_e32 v127, v127
	v_mul_f32_e64 v126, v126, -v112
	v_add_f32_e32 v128, v126, v126
	v_exp_f32_e32 v128, v128
	v_exp_f32_e32 v102, v102
	v_add_f32_e32 v98, v98, v106
	v_mul_f32_e32 v98, 0xbfb8aa3b, v98
	v_sub_f32_e32 v128, 1.0, v128
	v_max_f32_e32 v128, 0, v128
	v_sqrt_f32_e32 v128, v128
	v_add_f32_e32 v102, 1.0, v102
	v_rcp_f32_e32 v102, v102
	v_exp_f32_e32 v98, v98
	v_mul_f32_e32 v127, v127, v128
	v_mul_f32_e32 v127, v127, v136
	v_cvt_pk_bf16_f32 v132, v127, v126
	v_add_f32_e32 v126, v133, v117
	v_mul_f32_e32 v126, 0xbfb8aa3b, v126
	v_exp_f32_e32 v126, v126
	v_add_f32_e32 v127, v129, v109
	v_mul_f32_e32 v127, 0xbfb8aa3b, v127
	v_exp_f32_e32 v127, v127
	v_add_f32_e32 v126, 1.0, v126
	v_rcp_f32_e32 v126, v126
	v_and_b32_e32 v129, 0xffff0000, v212
	v_add_f32_e32 v127, 1.0, v127
	v_rcp_f32_e32 v127, v127
	v_mul_f32_e64 v126, v126, -v113
	v_add_f32_e32 v128, v126, v126
	v_exp_f32_e32 v128, v128
	v_mul_f32_e64 v102, v102, -v110
	v_add_f32_e32 v98, 1.0, v98
	v_rcp_f32_e32 v98, v98
	v_sub_f32_e32 v128, 1.0, v128
	v_max_f32_e32 v128, 0, v128
	v_sqrt_f32_e32 v128, v128
	v_add_f32_e32 v99, v99, v107
	v_mul_f32_e32 v99, 0xbfb8aa3b, v99
	v_exp_f32_e32 v99, v99
	v_mul_f32_e32 v127, v127, v128
	v_mul_f32_e32 v127, v127, v137
	v_cvt_pk_bf16_f32 v133, v127, v126
	v_lshlrev_b64 v[126:127], 12, v[210:211]
	v_lshl_add_u64 v[126:127], s[38:39], 0, v[126:127]
	v_lshl_add_u64 v[126:127], v[126:127], 0, v[186:187]
	flat_store_dwordx4 v[126:127], v[130:133]
	v_lshlrev_b32_e32 v128, 16, v212
	v_add_f32_e32 v99, 1.0, v99
	v_add_f32_e32 v132, v122, v122
	v_exp_f32_e32 v132, v132
	v_lshlrev_b32_e32 v130, 16, v213
	v_and_b32_e32 v131, 0xffff0000, v213
	v_rcp_f32_e32 v99, v99
	v_sub_f32_e32 v132, 1.0, v132
	v_max_f32_e32 v132, 0, v132
	v_sqrt_f32_e32 v132, v132
	v_add_f32_e32 v94, v94, v114
	v_mul_f32_e32 v94, 0xbfb8aa3b, v94
	v_exp_f32_e32 v94, v94
	v_mul_f32_e32 v118, v118, v132
	v_mul_f32_e32 v118, v118, v128
	v_cvt_pk_bf16_f32 v122, v118, v122
	v_add_f32_e32 v118, v123, v115
	v_mul_f32_e32 v118, 0xbfb8aa3b, v118
	v_exp_f32_e32 v118, v118
	v_add_f32_e32 v94, 1.0, v94
	v_rcp_f32_e32 v94, v94
	v_add_f32_e32 v90, v90, v106
	v_add_f32_e32 v118, 1.0, v118
	v_rcp_f32_e32 v118, v118
	v_mul_f32_e64 v94, v94, -v110
	v_mul_f32_e32 v90, 0xbfb8aa3b, v90
	v_exp_f32_e32 v90, v90
	v_mul_f32_e64 v118, v118, -v111
	v_add_f32_e32 v123, v118, v118
	v_exp_f32_e32 v123, v123
	v_add_f32_e32 v90, 1.0, v90
	v_rcp_f32_e32 v90, v90
	v_add_f32_e32 v91, v91, v107
	v_sub_f32_e32 v123, 1.0, v123
	v_max_f32_e32 v123, 0, v123
	v_sqrt_f32_e32 v123, v123
	v_mul_f32_e32 v91, 0xbfb8aa3b, v91
	v_exp_f32_e32 v91, v91
	v_add_f32_e32 v86, v86, v114
	v_mul_f32_e32 v119, v119, v123
	v_mul_f32_e32 v119, v119, v129
	v_cvt_pk_bf16_f32 v123, v119, v118
	v_add_f32_e32 v118, v124, v116
	v_mul_f32_e32 v118, 0xbfb8aa3b, v118
	v_exp_f32_e32 v118, v118
	v_add_f32_e32 v119, v120, v108
	v_mul_f32_e32 v119, 0xbfb8aa3b, v119
	v_exp_f32_e32 v119, v119
	v_add_f32_e32 v118, 1.0, v118
	v_rcp_f32_e32 v118, v118
	v_add_f32_e32 v91, 1.0, v91
	v_add_f32_e32 v119, 1.0, v119
	v_rcp_f32_e32 v119, v119
	v_mul_f32_e64 v118, v118, -v112
	v_add_f32_e32 v120, v118, v118
	v_exp_f32_e32 v120, v120
	v_rcp_f32_e32 v91, v91
	v_mul_f32_e32 v86, 0xbfb8aa3b, v86
	v_exp_f32_e32 v86, v86
	v_sub_f32_e32 v120, 1.0, v120
	v_max_f32_e32 v120, 0, v120
	v_sqrt_f32_e32 v120, v120
	v_add_f32_e32 v86, 1.0, v86
	v_rcp_f32_e32 v86, v86
	v_add_f32_e32 v82, v82, v106
	v_mul_f32_e32 v119, v119, v120
	v_mul_f32_e32 v119, v119, v130
	v_cvt_pk_bf16_f32 v124, v119, v118
	v_add_f32_e32 v118, v125, v117
	v_mul_f32_e32 v118, 0xbfb8aa3b, v118
	v_exp_f32_e32 v118, v118
	v_add_f32_e32 v119, v121, v109
	v_mul_f32_e32 v119, 0xbfb8aa3b, v119
	v_exp_f32_e32 v119, v119
	v_add_f32_e32 v118, 1.0, v118
	v_rcp_f32_e32 v118, v118
	v_and_b32_e32 v121, 0xffff0000, v208
	v_add_f32_e32 v119, 1.0, v119
	v_rcp_f32_e32 v119, v119
	v_mul_f32_e64 v118, v118, -v113
	v_add_f32_e32 v120, v118, v118
	v_exp_f32_e32 v120, v120
	v_mul_f32_e64 v86, v86, -v110
	v_mul_f32_e32 v82, 0xbfb8aa3b, v82
	v_exp_f32_e32 v82, v82
	v_sub_f32_e32 v120, 1.0, v120
	v_max_f32_e32 v120, 0, v120
	v_sqrt_f32_e32 v120, v120
	v_add_f32_e32 v82, 1.0, v82
	v_rcp_f32_e32 v82, v82
	v_add_f32_e32 v83, v83, v107
	v_mul_f32_e32 v119, v119, v120
	v_mul_f32_e32 v119, v119, v131
	v_cvt_pk_bf16_f32 v125, v119, v118
	v_lshlrev_b64 v[118:119], 12, v[206:207]
	v_lshl_add_u64 v[118:119], s[38:39], 0, v[118:119]
	v_lshl_add_u64 v[118:119], v[118:119], 0, v[186:187]
	flat_store_dwordx4 v[118:119], v[122:125]
	v_lshlrev_b32_e32 v120, 16, v208
	v_mul_f32_e32 v83, 0xbfb8aa3b, v83
	v_add_f32_e32 v124, v102, v102
	v_exp_f32_e32 v124, v124
	v_lshlrev_b32_e32 v122, 16, v209
	v_and_b32_e32 v123, 0xffff0000, v209
	v_exp_f32_e32 v83, v83
	v_sub_f32_e32 v124, 1.0, v124
	v_max_f32_e32 v124, 0, v124
	v_sqrt_f32_e32 v124, v124
	v_add_f32_e32 v83, 1.0, v83
	v_rcp_f32_e32 v83, v83
	v_add_f32_e32 v78, v78, v114
	v_mul_f32_e32 v98, v98, v124
	v_mul_f32_e32 v98, v98, v120
	v_cvt_pk_bf16_f32 v102, v98, v102
	v_add_f32_e32 v98, v103, v115
	v_mul_f32_e32 v98, 0xbfb8aa3b, v98
	v_exp_f32_e32 v98, v98
	v_mul_f32_e32 v78, 0xbfb8aa3b, v78
	v_exp_f32_e32 v78, v78
	v_add_f32_e32 v74, v74, v106
	v_add_f32_e32 v98, 1.0, v98
	v_rcp_f32_e32 v98, v98
	v_add_f32_e32 v78, 1.0, v78
	v_rcp_f32_e32 v78, v78
	v_mul_f32_e32 v74, 0xbfb8aa3b, v74
	v_mul_f32_e64 v98, v98, -v111
	v_add_f32_e32 v103, v98, v98
	v_exp_f32_e32 v103, v103
	v_mul_f32_e64 v78, v78, -v110
	v_exp_f32_e32 v74, v74
	v_add_f32_e32 v75, v75, v107
	v_sub_f32_e32 v103, 1.0, v103
	v_max_f32_e32 v103, 0, v103
	v_sqrt_f32_e32 v103, v103
	v_add_f32_e32 v74, 1.0, v74
	v_rcp_f32_e32 v74, v74
	v_mul_f32_e32 v75, 0xbfb8aa3b, v75
	v_mul_f32_e32 v99, v99, v103
	v_mul_f32_e32 v99, v99, v121
	v_cvt_pk_bf16_f32 v103, v99, v98
	v_add_f32_e32 v98, v104, v116
	v_mul_f32_e32 v98, 0xbfb8aa3b, v98
	v_exp_f32_e32 v98, v98
	v_add_f32_e32 v99, v100, v108
	v_mul_f32_e32 v99, 0xbfb8aa3b, v99
	v_exp_f32_e32 v99, v99
	v_add_f32_e32 v98, 1.0, v98
	v_rcp_f32_e32 v98, v98
	v_exp_f32_e32 v75, v75
	v_add_f32_e32 v99, 1.0, v99
	v_rcp_f32_e32 v99, v99
	v_mul_f32_e64 v98, v98, -v112
	v_add_f32_e32 v100, v98, v98
	v_exp_f32_e32 v100, v100
	v_add_f32_e32 v75, 1.0, v75
	v_rcp_f32_e32 v75, v75
	v_add_f32_e32 v76, v76, v108
	v_sub_f32_e32 v100, 1.0, v100
	v_max_f32_e32 v100, 0, v100
	v_sqrt_f32_e32 v100, v100
	v_mul_f32_e32 v76, 0xbfb8aa3b, v76
	v_exp_f32_e32 v76, v76
	v_add_f32_e32 v70, v70, v114
	v_mul_f32_e32 v99, v99, v100
	v_mul_f32_e32 v99, v99, v122
	v_cvt_pk_bf16_f32 v104, v99, v98
	v_add_f32_e32 v98, v105, v117
	v_mul_f32_e32 v98, 0xbfb8aa3b, v98
	v_exp_f32_e32 v98, v98
	v_add_f32_e32 v99, v101, v109
	v_mul_f32_e32 v99, 0xbfb8aa3b, v99
	v_exp_f32_e32 v99, v99
	v_add_f32_e32 v98, 1.0, v98
	v_rcp_f32_e32 v98, v98
	v_and_b32_e32 v101, 0xffff0000, v202
	v_add_f32_e32 v99, 1.0, v99
	v_rcp_f32_e32 v99, v99
	v_mul_f32_e64 v98, v98, -v113
	v_add_f32_e32 v100, v98, v98
	v_exp_f32_e32 v100, v100
	v_add_f32_e32 v76, 1.0, v76
	v_rcp_f32_e32 v76, v76
	v_mul_f32_e32 v70, 0xbfb8aa3b, v70
	v_sub_f32_e32 v100, 1.0, v100
	v_max_f32_e32 v100, 0, v100
	v_sqrt_f32_e32 v100, v100
	v_exp_f32_e32 v70, v70
	v_add_f32_e32 v77, v77, v109
	v_mul_f32_e32 v77, 0xbfb8aa3b, v77
	v_mul_f32_e32 v99, v99, v100
	v_mul_f32_e32 v99, v99, v123
	v_cvt_pk_bf16_f32 v105, v99, v98
	v_lshlrev_b64 v[98:99], 12, v[204:205]
	v_lshl_add_u64 v[98:99], s[38:39], 0, v[98:99]
	v_lshl_add_u64 v[98:99], v[98:99], 0, v[186:187]
	flat_store_dwordx4 v[98:99], v[102:105]
	v_lshlrev_b32_e32 v100, 16, v202
	v_add_f32_e32 v70, 1.0, v70
	v_add_f32_e32 v104, v94, v94
	v_exp_f32_e32 v104, v104
	v_lshlrev_b32_e32 v102, 16, v203
	v_and_b32_e32 v103, 0xffff0000, v203
	v_rcp_f32_e32 v70, v70
	v_sub_f32_e32 v104, 1.0, v104
	v_max_f32_e32 v104, 0, v104
	v_sqrt_f32_e32 v104, v104
	v_exp_f32_e32 v77, v77
	v_mul_f32_e64 v70, v70, -v110
	v_add_f32_e32 v66, v66, v106
	v_mul_f32_e32 v90, v90, v104
	v_mul_f32_e32 v90, v90, v100
	v_cvt_pk_bf16_f32 v94, v90, v94
	v_add_f32_e32 v90, v95, v115
	v_mul_f32_e32 v90, 0xbfb8aa3b, v90
	v_exp_f32_e32 v90, v90
	v_add_f32_e32 v77, 1.0, v77
	v_mul_f32_e32 v66, 0xbfb8aa3b, v66
	v_rcp_f32_e32 v77, v77
	v_add_f32_e32 v90, 1.0, v90
	v_rcp_f32_e32 v90, v90
	v_exp_f32_e32 v66, v66
	v_add_f32_e32 v67, v67, v107
	v_mul_f32_e32 v67, 0xbfb8aa3b, v67
	v_mul_f32_e64 v90, v90, -v111
	v_add_f32_e32 v95, v90, v90
	v_exp_f32_e32 v95, v95
	v_add_f32_e32 v66, 1.0, v66
	v_rcp_f32_e32 v66, v66
	v_exp_f32_e32 v67, v67
	v_sub_f32_e32 v95, 1.0, v95
	v_max_f32_e32 v95, 0, v95
	v_sqrt_f32_e32 v95, v95
	v_add_f32_e32 v67, 1.0, v67
	v_rcp_f32_e32 v67, v67
	v_add_f32_e32 v68, v68, v108
	v_mul_f32_e32 v91, v91, v95
	v_mul_f32_e32 v91, v91, v101
	v_cvt_pk_bf16_f32 v95, v91, v90
	v_add_f32_e32 v90, v96, v116
	v_mul_f32_e32 v90, 0xbfb8aa3b, v90
	v_exp_f32_e32 v90, v90
	v_add_f32_e32 v91, v92, v108
	v_mul_f32_e32 v91, 0xbfb8aa3b, v91
	v_exp_f32_e32 v91, v91
	v_add_f32_e32 v90, 1.0, v90
	v_rcp_f32_e32 v90, v90
	v_mul_f32_e32 v68, 0xbfb8aa3b, v68
	v_add_f32_e32 v91, 1.0, v91
	v_rcp_f32_e32 v91, v91
	v_mul_f32_e64 v90, v90, -v112
	v_add_f32_e32 v92, v90, v90
	v_exp_f32_e32 v92, v92
	v_exp_f32_e32 v68, v68
	v_add_f32_e32 v69, v69, v109
	v_mul_f32_e32 v69, 0xbfb8aa3b, v69
	v_sub_f32_e32 v92, 1.0, v92
	v_max_f32_e32 v92, 0, v92
	v_sqrt_f32_e32 v92, v92
	v_add_f32_e32 v68, 1.0, v68
	v_rcp_f32_e32 v68, v68
	v_exp_f32_e32 v69, v69
	v_mul_f32_e32 v91, v91, v92
	v_mul_f32_e32 v91, v91, v102
	v_cvt_pk_bf16_f32 v96, v91, v90
	v_add_f32_e32 v90, v97, v117
	v_mul_f32_e32 v90, 0xbfb8aa3b, v90
	v_exp_f32_e32 v90, v90
	v_add_f32_e32 v91, v93, v109
	v_mul_f32_e32 v91, 0xbfb8aa3b, v91
	v_exp_f32_e32 v91, v91
	v_add_f32_e32 v90, 1.0, v90
	v_rcp_f32_e32 v90, v90
	v_and_b32_e32 v93, 0xffff0000, v200
	v_add_f32_e32 v91, 1.0, v91
	v_rcp_f32_e32 v91, v91
	v_mul_f32_e64 v90, v90, -v113
	v_add_f32_e32 v92, v90, v90
	v_exp_f32_e32 v92, v92
	v_add_f32_e32 v69, 1.0, v69
	v_rcp_f32_e32 v69, v69
	v_sub_f32_e32 v92, 1.0, v92
	v_max_f32_e32 v92, 0, v92
	v_sqrt_f32_e32 v92, v92
	s_nop 0
	v_mul_f32_e32 v91, v91, v92
	v_mul_f32_e32 v91, v91, v103
	v_cvt_pk_bf16_f32 v97, v91, v90
	v_lshlrev_b64 v[90:91], 12, v[198:199]
	v_lshl_add_u64 v[90:91], s[38:39], 0, v[90:91]
	v_lshl_add_u64 v[90:91], v[90:91], 0, v[186:187]
	flat_store_dwordx4 v[90:91], v[94:97]
	v_lshlrev_b32_e32 v92, 16, v200
	s_nop 0
	v_add_f32_e32 v96, v86, v86
	v_exp_f32_e32 v96, v96
	v_lshlrev_b32_e32 v94, 16, v201
	v_and_b32_e32 v95, 0xffff0000, v201
	v_sub_f32_e32 v96, 1.0, v96
	v_max_f32_e32 v96, 0, v96
	v_sqrt_f32_e32 v96, v96
	s_nop 0
	v_mul_f32_e32 v82, v82, v96
	v_mul_f32_e32 v82, v82, v92
	v_cvt_pk_bf16_f32 v86, v82, v86
	v_add_f32_e32 v82, v87, v115
	v_mul_f32_e32 v82, 0xbfb8aa3b, v82
	v_exp_f32_e32 v82, v82
	s_nop 0
	v_add_f32_e32 v82, 1.0, v82
	v_rcp_f32_e32 v82, v82
	s_nop 0
	v_mul_f32_e64 v82, v82, -v111
	v_add_f32_e32 v87, v82, v82
	v_exp_f32_e32 v87, v87
	s_nop 0
	v_sub_f32_e32 v87, 1.0, v87
	v_max_f32_e32 v87, 0, v87
	v_sqrt_f32_e32 v87, v87
	s_nop 0
	v_mul_f32_e32 v83, v83, v87
	v_mul_f32_e32 v83, v83, v93
	v_cvt_pk_bf16_f32 v87, v83, v82
	v_add_f32_e32 v82, v88, v116
	v_mul_f32_e32 v82, 0xbfb8aa3b, v82
	v_exp_f32_e32 v82, v82
	v_add_f32_e32 v83, v84, v108
	v_mul_f32_e32 v83, 0xbfb8aa3b, v83
	v_exp_f32_e32 v83, v83
	v_add_f32_e32 v82, 1.0, v82
	v_rcp_f32_e32 v82, v82
	v_add_f32_e32 v83, 1.0, v83
	v_rcp_f32_e32 v83, v83
	v_mul_f32_e64 v82, v82, -v112
	v_add_f32_e32 v84, v82, v82
	v_exp_f32_e32 v84, v84
	s_nop 0
	v_sub_f32_e32 v84, 1.0, v84
	v_max_f32_e32 v84, 0, v84
	v_sqrt_f32_e32 v84, v84
	s_nop 0
	v_mul_f32_e32 v83, v83, v84
	v_mul_f32_e32 v83, v83, v94
	v_cvt_pk_bf16_f32 v88, v83, v82
	v_add_f32_e32 v82, v89, v117
	v_mul_f32_e32 v82, 0xbfb8aa3b, v82
	v_exp_f32_e32 v82, v82
	v_add_f32_e32 v83, v85, v109
	v_mul_f32_e32 v83, 0xbfb8aa3b, v83
	v_exp_f32_e32 v83, v83
	v_add_f32_e32 v82, 1.0, v82
	v_rcp_f32_e32 v82, v82
	v_and_b32_e32 v85, 0xffff0000, v196
	v_add_f32_e32 v83, 1.0, v83
	v_rcp_f32_e32 v83, v83
	v_mul_f32_e64 v82, v82, -v113
	v_add_f32_e32 v84, v82, v82
	v_exp_f32_e32 v84, v84
	s_nop 0
	v_sub_f32_e32 v84, 1.0, v84
	v_max_f32_e32 v84, 0, v84
	v_sqrt_f32_e32 v84, v84
	s_nop 0
	v_mul_f32_e32 v83, v83, v84
	v_mul_f32_e32 v83, v83, v95
	v_cvt_pk_bf16_f32 v89, v83, v82
	v_lshlrev_b64 v[82:83], 12, v[194:195]
	v_lshl_add_u64 v[82:83], s[38:39], 0, v[82:83]
	v_lshl_add_u64 v[82:83], v[82:83], 0, v[186:187]
	flat_store_dwordx4 v[82:83], v[86:89]
	v_lshlrev_b32_e32 v84, 16, v196
	s_nop 0
	v_add_f32_e32 v88, v78, v78
	v_exp_f32_e32 v88, v88
	v_lshlrev_b32_e32 v86, 16, v197
	v_and_b32_e32 v87, 0xffff0000, v197
	v_sub_f32_e32 v88, 1.0, v88
	v_max_f32_e32 v88, 0, v88
	v_sqrt_f32_e32 v88, v88
	s_nop 0
	v_mul_f32_e32 v74, v74, v88
	v_mul_f32_e32 v74, v74, v84
	v_cvt_pk_bf16_f32 v74, v74, v78
	v_add_f32_e32 v78, v79, v115
	v_mul_f32_e32 v78, 0xbfb8aa3b, v78
	v_exp_f32_e32 v78, v78
	v_lshlrev_b32_e32 v84, 16, v178
	v_add_f32_e32 v78, 1.0, v78
	v_rcp_f32_e32 v78, v78
	s_nop 0
	v_mul_f32_e64 v78, v78, -v111
	v_add_f32_e32 v79, v78, v78
	v_exp_f32_e32 v79, v79
	s_nop 0
	v_sub_f32_e32 v79, 1.0, v79
	v_max_f32_e32 v79, 0, v79
	v_sqrt_f32_e32 v79, v79
	s_nop 0
	v_mul_f32_e32 v75, v75, v79
	v_mul_f32_e32 v75, v75, v85
	v_cvt_pk_bf16_f32 v75, v75, v78
	v_add_f32_e32 v78, v80, v116
	v_mul_f32_e32 v78, 0xbfb8aa3b, v78
	v_exp_f32_e32 v78, v78
	v_add_f32_e32 v80, v70, v70
	v_exp_f32_e32 v80, v80
	v_and_b32_e32 v85, 0xffff0000, v178
	v_add_f32_e32 v78, 1.0, v78
	v_rcp_f32_e32 v78, v78
	v_sub_f32_e32 v80, 1.0, v80
	v_max_f32_e32 v80, 0, v80
	v_sqrt_f32_e32 v80, v80
	v_mul_f32_e64 v78, v78, -v112
	v_add_f32_e32 v79, v78, v78
	v_exp_f32_e32 v79, v79
	v_mul_f32_e32 v66, v66, v80
	v_sub_f32_e32 v79, 1.0, v79
	v_max_f32_e32 v79, 0, v79
	v_sqrt_f32_e32 v79, v79
	s_nop 0
	v_mul_f32_e32 v76, v76, v79
	v_mul_f32_e32 v76, v76, v86
	v_cvt_pk_bf16_f32 v76, v76, v78
	v_add_f32_e32 v78, v81, v117
	v_mul_f32_e32 v78, 0xbfb8aa3b, v78
	v_exp_f32_e32 v78, v78
	v_lshlrev_b32_e32 v86, 16, v179
	v_add_f32_e32 v78, 1.0, v78
	v_rcp_f32_e32 v78, v78
	s_nop 0
	v_mul_f32_e64 v78, v78, -v113
	v_add_f32_e32 v79, v78, v78
	v_exp_f32_e32 v79, v79
	s_nop 0
	v_sub_f32_e32 v79, 1.0, v79
	v_max_f32_e32 v79, 0, v79
	v_sqrt_f32_e32 v79, v79
	s_nop 0
	v_mul_f32_e32 v77, v77, v79
	v_mul_f32_e32 v77, v77, v87
	v_cvt_pk_bf16_f32 v77, v77, v78
	v_lshlrev_b64 v[78:79], 12, v[190:191]
	v_lshl_add_u64 v[78:79], s[38:39], 0, v[78:79]
	v_lshl_add_u64 v[78:79], v[78:79], 0, v[186:187]
	flat_store_dwordx4 v[78:79], v[74:77]
	v_and_b32_e32 v87, 0xffff0000, v179
	s_nop 0
	v_lshlrev_b32_e32 v74, 16, v192
	v_mul_f32_e32 v66, v66, v74
	v_cvt_pk_bf16_f32 v66, v66, v70
	v_add_f32_e32 v70, v71, v115
	v_mul_f32_e32 v70, 0xbfb8aa3b, v70
	v_exp_f32_e32 v70, v70
	v_and_b32_e32 v75, 0xffff0000, v192
	v_lshlrev_b32_e32 v76, 16, v193
	v_and_b32_e32 v77, 0xffff0000, v193
	v_add_f32_e32 v70, 1.0, v70
	v_rcp_f32_e32 v70, v70
	s_nop 0
	v_mul_f32_e64 v70, v70, -v111
	v_add_f32_e32 v71, v70, v70
	v_exp_f32_e32 v71, v71
	s_nop 0
	v_sub_f32_e32 v71, 1.0, v71
	v_max_f32_e32 v71, 0, v71
	v_sqrt_f32_e32 v71, v71
	s_nop 0
	v_mul_f32_e32 v67, v67, v71
	v_mul_f32_e32 v67, v67, v75
	v_cvt_pk_bf16_f32 v67, v67, v70
	v_add_f32_e32 v70, v72, v116
	v_mul_f32_e32 v70, 0xbfb8aa3b, v70
	v_exp_f32_e32 v70, v70
	s_nop 0
	v_add_f32_e32 v70, 1.0, v70
	v_rcp_f32_e32 v70, v70
	s_nop 0
	v_mul_f32_e64 v70, v70, -v112
	v_add_f32_e32 v71, v70, v70
	v_exp_f32_e32 v71, v71
	s_nop 0
	v_sub_f32_e32 v71, 1.0, v71
	v_max_f32_e32 v71, 0, v71
	v_sqrt_f32_e32 v71, v71
	s_nop 0
	v_mul_f32_e32 v68, v68, v71
	v_mul_f32_e32 v68, v68, v76
	v_cvt_pk_bf16_f32 v68, v68, v70
	v_add_f32_e32 v70, v73, v117
	v_mul_f32_e32 v70, 0xbfb8aa3b, v70
	v_exp_f32_e32 v70, v70
	s_nop 0
	v_add_f32_e32 v70, 1.0, v70
	v_rcp_f32_e32 v70, v70
	s_nop 0
	v_mul_f32_e64 v70, v70, -v113
	v_add_f32_e32 v71, v70, v70
	v_exp_f32_e32 v71, v71
	s_nop 0
	v_sub_f32_e32 v71, 1.0, v71
	v_max_f32_e32 v71, 0, v71
	v_sqrt_f32_e32 v71, v71
	s_nop 0
	v_mul_f32_e32 v69, v69, v71
	v_mul_f32_e32 v69, v69, v77
	v_cvt_pk_bf16_f32 v69, v69, v70
	v_lshlrev_b64 v[70:71], 12, v[180:181]
	v_lshl_add_u64 v[70:71], s[38:39], 0, v[70:71]
	v_lshl_add_u64 v[80:81], v[70:71], 0, v[186:187]
	flat_store_dwordx4 v[80:81], v[66:69]
	s_nop 1
	v_mov_b64_e32 v[74:75], v[234:235]
	v_mov_b64_e32 v[76:77], v[236:237]
	v_mov_b64_e32 v[70:71], v[238:239]
	v_mov_b64_e32 v[72:73], v[240:241]
	v_mov_b64_e32 v[66:67], v[242:243]
	v_mov_b64_e32 v[68:69], v[244:245]
	v_add_f32_e32 v62, v62, v74
	v_mul_f32_e32 v62, 0xbfb8aa3b, v62
	v_exp_f32_e32 v62, v62
	v_add_f32_e32 v58, v58, v70
	v_mul_f32_e32 v58, 0xbfb8aa3b, v58
	v_exp_f32_e32 v58, v58
	v_add_f32_e32 v62, 1.0, v62
	v_rcp_f32_e32 v62, v62
	v_add_f32_e32 v59, v59, v71
	v_add_f32_e32 v58, 1.0, v58
	v_rcp_f32_e32 v58, v58
	v_mul_f32_e64 v62, v62, -v66
	v_add_f32_e32 v88, v62, v62
	v_exp_f32_e32 v88, v88
	v_mul_f32_e32 v59, 0xbfb8aa3b, v59
	v_exp_f32_e32 v59, v59
	v_add_f32_e32 v60, v60, v72
	v_sub_f32_e32 v88, 1.0, v88
	v_max_f32_e32 v88, 0, v88
	v_sqrt_f32_e32 v88, v88
	v_add_f32_e32 v59, 1.0, v59
	v_rcp_f32_e32 v59, v59
	v_mul_f32_e32 v60, 0xbfb8aa3b, v60
	v_mul_f32_e32 v58, v58, v88
	v_mul_f32_e32 v58, v58, v84
	v_cvt_pk_bf16_f32 v58, v58, v62
	v_add_f32_e32 v62, v63, v75
	v_mul_f32_e32 v62, 0xbfb8aa3b, v62
	v_exp_f32_e32 v62, v62
	v_exp_f32_e32 v60, v60
	v_add_f32_e32 v61, v61, v73
	v_mul_f32_e32 v61, 0xbfb8aa3b, v61
	v_add_f32_e32 v62, 1.0, v62
	v_rcp_f32_e32 v62, v62
	v_add_f32_e32 v60, 1.0, v60
	v_rcp_f32_e32 v60, v60
	v_add_f32_e32 v54, v54, v74
	v_mul_f32_e64 v62, v62, -v67
	v_add_f32_e32 v63, v62, v62
	v_exp_f32_e32 v63, v63
	v_exp_f32_e32 v61, v61
	v_mul_f32_e32 v54, 0xbfb8aa3b, v54
	v_exp_f32_e32 v54, v54
	v_sub_f32_e32 v63, 1.0, v63
	v_max_f32_e32 v63, 0, v63
	v_sqrt_f32_e32 v63, v63
	v_add_f32_e32 v61, 1.0, v61
	v_rcp_f32_e32 v61, v61
	v_add_f32_e32 v54, 1.0, v54
	v_mul_f32_e32 v59, v59, v63
	v_mul_f32_e32 v59, v59, v85
	v_cvt_pk_bf16_f32 v59, v59, v62
	v_add_f32_e32 v62, v64, v76
	v_mul_f32_e32 v62, 0xbfb8aa3b, v62
	v_exp_f32_e32 v62, v62
	v_rcp_f32_e32 v54, v54
	v_add_f32_e32 v50, v50, v70
	v_mul_f32_e32 v50, 0xbfb8aa3b, v50
	v_add_f32_e32 v62, 1.0, v62
	v_rcp_f32_e32 v62, v62
	v_mul_f32_e64 v54, v54, -v66
	v_exp_f32_e32 v50, v50
	v_add_f32_e32 v51, v51, v71
	v_mul_f32_e64 v62, v62, -v68
	v_add_f32_e32 v63, v62, v62
	v_exp_f32_e32 v63, v63
	v_add_f32_e32 v50, 1.0, v50
	v_rcp_f32_e32 v50, v50
	v_mul_f32_e32 v51, 0xbfb8aa3b, v51
	v_sub_f32_e32 v63, 1.0, v63
	v_max_f32_e32 v63, 0, v63
	v_sqrt_f32_e32 v63, v63
	v_exp_f32_e32 v51, v51
	v_add_f32_e32 v52, v52, v72
	v_mul_f32_e32 v52, 0xbfb8aa3b, v52
	v_mul_f32_e32 v60, v60, v63
	v_mul_f32_e32 v60, v60, v86
	v_cvt_pk_bf16_f32 v60, v60, v62
	v_add_f32_e32 v62, v65, v77
	v_mul_f32_e32 v62, 0xbfb8aa3b, v62
	v_exp_f32_e32 v62, v62
	v_add_f32_e32 v51, 1.0, v51
	v_rcp_f32_e32 v51, v51
	v_exp_f32_e32 v52, v52
	v_add_f32_e32 v62, 1.0, v62
	v_rcp_f32_e32 v62, v62
	v_add_f32_e32 v53, v53, v73
	v_add_f32_e32 v52, 1.0, v52
	v_rcp_f32_e32 v52, v52
	v_mul_f32_e64 v62, v62, -v69
	v_add_f32_e32 v63, v62, v62
	v_exp_f32_e32 v63, v63
	v_mul_f32_e32 v53, 0xbfb8aa3b, v53
	v_add_f32_e32 v46, v46, v74
	v_exp_f32_e32 v53, v53
	v_sub_f32_e32 v63, 1.0, v63
	v_max_f32_e32 v63, 0, v63
	v_sqrt_f32_e32 v63, v63
	v_mul_f32_e32 v46, 0xbfb8aa3b, v46
	v_exp_f32_e32 v46, v46
	v_add_f32_e32 v53, 1.0, v53
	v_mul_f32_e32 v61, v61, v63
	v_mul_f32_e32 v61, v61, v87
	v_cvt_pk_bf16_f32 v61, v61, v62
	v_add_f32_e32 v62, v54, v54
	v_exp_f32_e32 v62, v62
	flat_store_dwordx4 v[138:139], v[58:61] offset:64
	v_rcp_f32_e32 v53, v53
	v_add_f32_e32 v46, 1.0, v46
	v_sub_f32_e32 v62, 1.0, v62
	v_max_f32_e32 v62, 0, v62
	v_sqrt_f32_e32 v62, v62
	v_lshlrev_b32_e32 v58, 16, v164
	v_and_b32_e32 v59, 0xffff0000, v164
	v_lshlrev_b32_e32 v60, 16, v165
	v_mul_f32_e32 v50, v50, v62
	v_mul_f32_e32 v50, v50, v58
	v_cvt_pk_bf16_f32 v50, v50, v54
	v_add_f32_e32 v54, v55, v75
	v_mul_f32_e32 v54, 0xbfb8aa3b, v54
	v_exp_f32_e32 v54, v54
	v_rcp_f32_e32 v46, v46
	v_and_b32_e32 v61, 0xffff0000, v165
	v_add_f32_e32 v42, v42, v70
	v_add_f32_e32 v54, 1.0, v54
	v_rcp_f32_e32 v54, v54
	v_mul_f32_e64 v46, v46, -v66
	v_mul_f32_e32 v42, 0xbfb8aa3b, v42
	v_exp_f32_e32 v42, v42
	v_mul_f32_e64 v54, v54, -v67
	v_add_f32_e32 v55, v54, v54
	v_exp_f32_e32 v55, v55
	v_add_f32_e32 v42, 1.0, v42
	v_rcp_f32_e32 v42, v42
	v_add_f32_e32 v43, v43, v71
	v_sub_f32_e32 v55, 1.0, v55
	v_max_f32_e32 v55, 0, v55
	v_sqrt_f32_e32 v55, v55
	v_mul_f32_e32 v43, 0xbfb8aa3b, v43
	v_exp_f32_e32 v43, v43
	v_add_f32_e32 v44, v44, v72
	v_mul_f32_e32 v51, v51, v55
	v_mul_f32_e32 v51, v51, v59
	v_cvt_pk_bf16_f32 v51, v51, v54
	v_add_f32_e32 v54, v56, v76
	v_mul_f32_e32 v54, 0xbfb8aa3b, v54
	v_exp_f32_e32 v54, v54
	v_add_f32_e32 v43, 1.0, v43
	v_rcp_f32_e32 v43, v43
	v_mul_f32_e32 v44, 0xbfb8aa3b, v44
	v_add_f32_e32 v54, 1.0, v54
	v_rcp_f32_e32 v54, v54
	v_exp_f32_e32 v44, v44
	v_add_f32_e32 v45, v45, v73
	v_mul_f32_e32 v45, 0xbfb8aa3b, v45
	v_mul_f32_e64 v54, v54, -v68
	v_add_f32_e32 v55, v54, v54
	v_exp_f32_e32 v55, v55
	v_add_f32_e32 v44, 1.0, v44
	v_rcp_f32_e32 v44, v44
	v_add_f32_e32 v38, v38, v74
	v_sub_f32_e32 v55, 1.0, v55
	v_max_f32_e32 v55, 0, v55
	v_sqrt_f32_e32 v55, v55
	v_exp_f32_e32 v45, v45
	v_mul_f32_e32 v38, 0xbfb8aa3b, v38
	v_exp_f32_e32 v38, v38
	v_mul_f32_e32 v52, v52, v55
	v_mul_f32_e32 v52, v52, v60
	v_cvt_pk_bf16_f32 v52, v52, v54
	v_add_f32_e32 v54, v57, v77
	v_mul_f32_e32 v54, 0xbfb8aa3b, v54
	v_exp_f32_e32 v54, v54
	v_add_f32_e32 v45, 1.0, v45
	v_rcp_f32_e32 v45, v45
	v_add_f32_e32 v38, 1.0, v38
	v_add_f32_e32 v54, 1.0, v54
	v_rcp_f32_e32 v54, v54
	v_rcp_f32_e32 v38, v38
	v_add_f32_e32 v34, v34, v70
	v_mul_f32_e32 v34, 0xbfb8aa3b, v34
	v_mul_f32_e64 v54, v54, -v69
	v_add_f32_e32 v55, v54, v54
	v_exp_f32_e32 v55, v55
	v_mul_f32_e64 v38, v38, -v66
	v_exp_f32_e32 v34, v34
	v_add_f32_e32 v35, v35, v71
	v_sub_f32_e32 v55, 1.0, v55
	v_max_f32_e32 v55, 0, v55
	v_sqrt_f32_e32 v55, v55
	v_add_f32_e32 v34, 1.0, v34
	v_rcp_f32_e32 v34, v34
	v_mul_f32_e32 v35, 0xbfb8aa3b, v35
	v_mul_f32_e32 v53, v53, v55
	v_mul_f32_e32 v53, v53, v61
	v_cvt_pk_bf16_f32 v53, v53, v54
	v_add_f32_e32 v54, v46, v46
	v_exp_f32_e32 v54, v54
	flat_store_dwordx4 v[126:127], v[50:53] offset:64
	v_exp_f32_e32 v35, v35
	v_sub_f32_e32 v54, 1.0, v54
	v_max_f32_e32 v54, 0, v54
	v_sqrt_f32_e32 v54, v54
	v_lshlrev_b32_e32 v50, 16, v162
	v_and_b32_e32 v51, 0xffff0000, v162
	v_lshlrev_b32_e32 v52, 16, v163
	v_mul_f32_e32 v42, v42, v54
	v_mul_f32_e32 v42, v42, v50
	v_cvt_pk_bf16_f32 v42, v42, v46
	v_add_f32_e32 v46, v47, v75
	v_mul_f32_e32 v46, 0xbfb8aa3b, v46
	v_exp_f32_e32 v46, v46
	v_and_b32_e32 v53, 0xffff0000, v163
	v_add_f32_e32 v35, 1.0, v35
	v_rcp_f32_e32 v35, v35
	v_add_f32_e32 v46, 1.0, v46
	v_rcp_f32_e32 v46, v46
	v_add_f32_e32 v36, v36, v72
	v_mul_f32_e32 v36, 0xbfb8aa3b, v36
	v_exp_f32_e32 v36, v36
	v_mul_f32_e64 v46, v46, -v67
	v_add_f32_e32 v47, v46, v46
	v_exp_f32_e32 v47, v47
	v_add_f32_e32 v36, 1.0, v36
	v_rcp_f32_e32 v36, v36
	v_add_f32_e32 v37, v37, v73
	v_sub_f32_e32 v47, 1.0, v47
	v_max_f32_e32 v47, 0, v47
	v_sqrt_f32_e32 v47, v47
	v_mul_f32_e32 v37, 0xbfb8aa3b, v37
	v_add_f32_e32 v30, v30, v74
	v_exp_f32_e32 v37, v37
	v_mul_f32_e32 v43, v43, v47
	v_mul_f32_e32 v43, v43, v51
	v_cvt_pk_bf16_f32 v43, v43, v46
	v_add_f32_e32 v46, v48, v76
	v_mul_f32_e32 v46, 0xbfb8aa3b, v46
	v_exp_f32_e32 v46, v46
	v_mul_f32_e32 v30, 0xbfb8aa3b, v30
	v_exp_f32_e32 v30, v30
	v_add_f32_e32 v37, 1.0, v37
	v_add_f32_e32 v46, 1.0, v46
	v_rcp_f32_e32 v46, v46
	v_rcp_f32_e32 v37, v37
	v_add_f32_e32 v30, 1.0, v30
	v_rcp_f32_e32 v30, v30
	v_mul_f32_e64 v46, v46, -v68
	v_add_f32_e32 v47, v46, v46
	v_exp_f32_e32 v47, v47
	v_mul_f32_e64 v30, v30, -v66
	v_add_f32_e32 v26, v26, v70
	v_mul_f32_e32 v26, 0xbfb8aa3b, v26
	v_sub_f32_e32 v47, 1.0, v47
	v_max_f32_e32 v47, 0, v47
	v_sqrt_f32_e32 v47, v47
	v_exp_f32_e32 v26, v26
	v_add_f32_e32 v27, v27, v71
	v_mul_f32_e32 v27, 0xbfb8aa3b, v27
	v_mul_f32_e32 v44, v44, v47
	v_mul_f32_e32 v44, v44, v52
	v_cvt_pk_bf16_f32 v44, v44, v46
	v_add_f32_e32 v46, v49, v77
	v_mul_f32_e32 v46, 0xbfb8aa3b, v46
	v_exp_f32_e32 v46, v46
	v_add_f32_e32 v26, 1.0, v26
	v_rcp_f32_e32 v26, v26
	v_exp_f32_e32 v27, v27
	v_add_f32_e32 v46, 1.0, v46
	v_rcp_f32_e32 v46, v46
	v_add_f32_e32 v28, v28, v72
	v_add_f32_e32 v27, 1.0, v27
	v_rcp_f32_e32 v27, v27
	v_mul_f32_e64 v46, v46, -v69
	v_add_f32_e32 v47, v46, v46
	v_exp_f32_e32 v47, v47
	v_mul_f32_e32 v28, 0xbfb8aa3b, v28
	v_exp_f32_e32 v28, v28
	v_add_f32_e32 v29, v29, v73
	v_sub_f32_e32 v47, 1.0, v47
	v_max_f32_e32 v47, 0, v47
	v_sqrt_f32_e32 v47, v47
	v_add_f32_e32 v28, 1.0, v28
	v_rcp_f32_e32 v28, v28
	v_mul_f32_e32 v29, 0xbfb8aa3b, v29
	v_mul_f32_e32 v45, v45, v47
	v_mul_f32_e32 v45, v45, v53
	v_cvt_pk_bf16_f32 v45, v45, v46
	v_add_f32_e32 v46, v38, v38
	v_exp_f32_e32 v46, v46
	flat_store_dwordx4 v[118:119], v[42:45] offset:64
	v_add_f32_e32 v22, v22, v74
	v_exp_f32_e32 v29, v29
	v_sub_f32_e32 v46, 1.0, v46
	v_max_f32_e32 v46, 0, v46
	v_sqrt_f32_e32 v46, v46
	v_lshlrev_b32_e32 v42, 16, v160
	v_and_b32_e32 v43, 0xffff0000, v160
	v_lshlrev_b32_e32 v44, 16, v161
	v_mul_f32_e32 v34, v34, v46
	v_mul_f32_e32 v34, v34, v42
	v_cvt_pk_bf16_f32 v34, v34, v38
	v_add_f32_e32 v38, v39, v75
	v_mul_f32_e32 v38, 0xbfb8aa3b, v38
	v_exp_f32_e32 v38, v38
	v_and_b32_e32 v45, 0xffff0000, v161
	v_mul_f32_e32 v22, 0xbfb8aa3b, v22
	v_exp_f32_e32 v22, v22
	v_add_f32_e32 v38, 1.0, v38
	v_rcp_f32_e32 v38, v38
	v_add_f32_e32 v29, 1.0, v29
	v_rcp_f32_e32 v29, v29
	v_add_f32_e32 v22, 1.0, v22
	v_mul_f32_e64 v38, v38, -v67
	v_add_f32_e32 v39, v38, v38
	v_exp_f32_e32 v39, v39
	v_rcp_f32_e32 v22, v22
	v_add_f32_e32 v18, v18, v70
	v_mul_f32_e32 v18, 0xbfb8aa3b, v18
	v_sub_f32_e32 v39, 1.0, v39
	v_max_f32_e32 v39, 0, v39
	v_sqrt_f32_e32 v39, v39
	v_mul_f32_e64 v22, v22, -v66
	v_exp_f32_e32 v18, v18
	v_add_f32_e32 v19, v19, v71
	v_mul_f32_e32 v35, v35, v39
	v_mul_f32_e32 v35, v35, v43
	v_cvt_pk_bf16_f32 v35, v35, v38
	v_add_f32_e32 v38, v40, v76
	v_mul_f32_e32 v38, 0xbfb8aa3b, v38
	v_exp_f32_e32 v38, v38
	v_add_f32_e32 v18, 1.0, v18
	v_rcp_f32_e32 v18, v18
	v_mul_f32_e32 v19, 0xbfb8aa3b, v19
	v_add_f32_e32 v38, 1.0, v38
	v_rcp_f32_e32 v38, v38
	v_exp_f32_e32 v19, v19
	v_add_f32_e32 v20, v20, v72
	v_mul_f32_e32 v20, 0xbfb8aa3b, v20
	v_mul_f32_e64 v38, v38, -v68
	v_add_f32_e32 v39, v38, v38
	v_exp_f32_e32 v39, v39
	v_add_f32_e32 v19, 1.0, v19
	v_rcp_f32_e32 v19, v19
	v_exp_f32_e32 v20, v20
	v_sub_f32_e32 v39, 1.0, v39
	v_max_f32_e32 v39, 0, v39
	v_sqrt_f32_e32 v39, v39
	v_add_f32_e32 v20, 1.0, v20
	v_rcp_f32_e32 v20, v20
	v_add_f32_e32 v21, v21, v73
	v_mul_f32_e32 v36, v36, v39
	v_mul_f32_e32 v36, v36, v44
	v_cvt_pk_bf16_f32 v36, v36, v38
	v_add_f32_e32 v38, v41, v77
	v_mul_f32_e32 v38, 0xbfb8aa3b, v38
	v_exp_f32_e32 v38, v38
	v_mul_f32_e32 v21, 0xbfb8aa3b, v21
	v_add_f32_e32 v14, v14, v74
	v_exp_f32_e32 v21, v21
	v_add_f32_e32 v38, 1.0, v38
	v_rcp_f32_e32 v38, v38
	v_mul_f32_e32 v14, 0xbfb8aa3b, v14
	v_exp_f32_e32 v14, v14
	v_add_f32_e32 v21, 1.0, v21
	v_mul_f32_e64 v38, v38, -v69
	v_add_f32_e32 v39, v38, v38
	v_exp_f32_e32 v39, v39
	v_rcp_f32_e32 v21, v21
	v_add_f32_e32 v14, 1.0, v14
	v_rcp_f32_e32 v14, v14
	v_sub_f32_e32 v39, 1.0, v39
	v_max_f32_e32 v39, 0, v39
	v_sqrt_f32_e32 v39, v39
	v_mul_f32_e64 v14, v14, -v66
	v_add_f32_e32 v10, v10, v70
	v_mul_f32_e32 v10, 0xbfb8aa3b, v10
	v_mul_f32_e32 v37, v37, v39
	v_mul_f32_e32 v37, v37, v45
	v_cvt_pk_bf16_f32 v37, v37, v38
	v_add_f32_e32 v38, v30, v30
	v_exp_f32_e32 v38, v38
	flat_store_dwordx4 v[98:99], v[34:37] offset:64
	v_exp_f32_e32 v10, v10
	v_sub_f32_e32 v38, 1.0, v38
	v_max_f32_e32 v38, 0, v38
	v_sqrt_f32_e32 v38, v38
	v_lshlrev_b32_e32 v34, 16, v158
	v_and_b32_e32 v35, 0xffff0000, v158
	v_lshlrev_b32_e32 v36, 16, v159
	v_mul_f32_e32 v26, v26, v38
	v_mul_f32_e32 v26, v26, v34
	v_cvt_pk_bf16_f32 v26, v26, v30
	v_add_f32_e32 v30, v31, v75
	v_mul_f32_e32 v30, 0xbfb8aa3b, v30
	v_exp_f32_e32 v30, v30
	v_and_b32_e32 v37, 0xffff0000, v159
	v_add_f32_e32 v10, 1.0, v10
	v_rcp_f32_e32 v10, v10
	v_add_f32_e32 v30, 1.0, v30
	v_rcp_f32_e32 v30, v30
	v_add_f32_e32 v11, v11, v71
	v_mul_f32_e32 v11, 0xbfb8aa3b, v11
	v_exp_f32_e32 v11, v11
	v_mul_f32_e64 v30, v30, -v67
	v_add_f32_e32 v31, v30, v30
	v_exp_f32_e32 v31, v31
	v_add_f32_e32 v11, 1.0, v11
	v_rcp_f32_e32 v11, v11
	v_add_f32_e32 v12, v12, v72
	v_sub_f32_e32 v31, 1.0, v31
	v_max_f32_e32 v31, 0, v31
	v_sqrt_f32_e32 v31, v31
	v_mul_f32_e32 v12, 0xbfb8aa3b, v12
	v_exp_f32_e32 v12, v12
	v_add_f32_e32 v13, v13, v73
	v_mul_f32_e32 v27, v27, v31
	v_mul_f32_e32 v27, v27, v35
	v_cvt_pk_bf16_f32 v27, v27, v30
	v_add_f32_e32 v30, v32, v76
	v_mul_f32_e32 v30, 0xbfb8aa3b, v30
	v_exp_f32_e32 v30, v30
	v_add_f32_e32 v12, 1.0, v12
	v_rcp_f32_e32 v12, v12
	v_mul_f32_e32 v13, 0xbfb8aa3b, v13
	v_add_f32_e32 v30, 1.0, v30
	v_rcp_f32_e32 v30, v30
	v_add_f32_e32 v6, v6, v74
	v_exp_f32_e32 v13, v13
	v_mul_f32_e32 v6, 0xbfb8aa3b, v6
	v_mul_f32_e64 v30, v30, -v68
	v_add_f32_e32 v31, v30, v30
	v_exp_f32_e32 v31, v31
	v_exp_f32_e32 v6, v6
	v_add_f32_e32 v13, 1.0, v13
	v_rcp_f32_e32 v13, v13
	v_sub_f32_e32 v31, 1.0, v31
	v_max_f32_e32 v31, 0, v31
	v_sqrt_f32_e32 v31, v31
	v_add_f32_e32 v6, 1.0, v6
	v_rcp_f32_e32 v6, v6
	v_add_f32_e32 v2, v2, v70
	v_mul_f32_e32 v28, v28, v31
	v_mul_f32_e32 v28, v28, v36
	v_cvt_pk_bf16_f32 v28, v28, v30
	v_add_f32_e32 v30, v33, v77
	v_mul_f32_e32 v30, 0xbfb8aa3b, v30
	v_exp_f32_e32 v30, v30
	v_mul_f32_e64 v6, v6, -v66
	v_mul_f32_e32 v2, 0xbfb8aa3b, v2
	v_exp_f32_e32 v2, v2
	v_add_f32_e32 v30, 1.0, v30
	v_rcp_f32_e32 v30, v30
	v_add_f32_e32 v3, v3, v71
	v_add_f32_e32 v2, 1.0, v2
	v_rcp_f32_e32 v2, v2
	v_mul_f32_e64 v30, v30, -v69
	v_add_f32_e32 v31, v30, v30
	v_exp_f32_e32 v31, v31
	v_mul_f32_e32 v3, 0xbfb8aa3b, v3
	v_exp_f32_e32 v3, v3
	v_add_f32_e32 v4, v4, v72
	v_sub_f32_e32 v31, 1.0, v31
	v_max_f32_e32 v31, 0, v31
	v_sqrt_f32_e32 v31, v31
	v_add_f32_e32 v3, 1.0, v3
	v_rcp_f32_e32 v3, v3
	v_mul_f32_e32 v4, 0xbfb8aa3b, v4
	v_mul_f32_e32 v29, v29, v31
	v_mul_f32_e32 v29, v29, v37
	v_cvt_pk_bf16_f32 v29, v29, v30
	v_add_f32_e32 v30, v22, v22
	v_exp_f32_e32 v30, v30
	flat_store_dwordx4 v[90:91], v[26:29] offset:64
	v_exp_f32_e32 v4, v4
	v_add_f32_e32 v5, v5, v73
	v_sub_f32_e32 v30, 1.0, v30
	v_max_f32_e32 v30, 0, v30
	v_sqrt_f32_e32 v30, v30
	v_lshlrev_b32_e32 v26, 16, v156
	v_and_b32_e32 v27, 0xffff0000, v156
	v_lshlrev_b32_e32 v28, 16, v157
	v_mul_f32_e32 v18, v18, v30
	v_mul_f32_e32 v18, v18, v26
	v_cvt_pk_bf16_f32 v18, v18, v22
	v_add_f32_e32 v22, v23, v75
	v_mul_f32_e32 v22, 0xbfb8aa3b, v22
	v_exp_f32_e32 v22, v22
	v_and_b32_e32 v29, 0xffff0000, v157
	v_add_f32_e32 v4, 1.0, v4
	v_rcp_f32_e32 v4, v4
	v_add_f32_e32 v22, 1.0, v22
	v_rcp_f32_e32 v22, v22
	v_mul_f32_e32 v5, 0xbfb8aa3b, v5
	v_exp_f32_e32 v5, v5
	v_mul_f32_e64 v22, v22, -v67
	v_add_f32_e32 v23, v22, v22
	v_exp_f32_e32 v23, v23
	v_add_f32_e32 v5, 1.0, v5
	v_rcp_f32_e32 v5, v5
	v_sub_f32_e32 v23, 1.0, v23
	v_max_f32_e32 v23, 0, v23
	v_sqrt_f32_e32 v23, v23
	s_nop 0
	v_mul_f32_e32 v19, v19, v23
	v_mul_f32_e32 v19, v19, v27
	v_cvt_pk_bf16_f32 v19, v19, v22
	v_add_f32_e32 v22, v24, v76
	v_mul_f32_e32 v22, 0xbfb8aa3b, v22
	v_exp_f32_e32 v22, v22
	s_nop 0
	v_add_f32_e32 v22, 1.0, v22
	v_rcp_f32_e32 v22, v22
	s_nop 0
	v_mul_f32_e64 v22, v22, -v68
	v_add_f32_e32 v23, v22, v22
	v_exp_f32_e32 v23, v23
	s_nop 0
	v_sub_f32_e32 v23, 1.0, v23
	v_max_f32_e32 v23, 0, v23
	v_sqrt_f32_e32 v23, v23
	s_nop 0
	v_mul_f32_e32 v20, v20, v23
	v_mul_f32_e32 v20, v20, v28
	v_cvt_pk_bf16_f32 v20, v20, v22
	v_add_f32_e32 v22, v25, v77
	v_mul_f32_e32 v22, 0xbfb8aa3b, v22
	v_exp_f32_e32 v22, v22
	s_nop 0
	v_add_f32_e32 v22, 1.0, v22
	v_rcp_f32_e32 v22, v22
	s_nop 0
	v_mul_f32_e64 v22, v22, -v69
	v_add_f32_e32 v23, v22, v22
	v_exp_f32_e32 v23, v23
	s_nop 0
	v_sub_f32_e32 v23, 1.0, v23
	v_max_f32_e32 v23, 0, v23
	v_sqrt_f32_e32 v23, v23
	s_nop 0
	v_mul_f32_e32 v21, v21, v23
	v_mul_f32_e32 v21, v21, v29
	v_cvt_pk_bf16_f32 v21, v21, v22
	v_add_f32_e32 v22, v14, v14
	v_exp_f32_e32 v22, v22
	flat_store_dwordx4 v[82:83], v[18:21] offset:64
	v_sub_f32_e32 v22, 1.0, v22
	v_max_f32_e32 v22, 0, v22
	v_sqrt_f32_e32 v22, v22
	v_lshlrev_b32_e32 v18, 16, v154
	v_and_b32_e32 v19, 0xffff0000, v154
	v_lshlrev_b32_e32 v20, 16, v155
	v_mul_f32_e32 v10, v10, v22
	v_mul_f32_e32 v10, v10, v18
	v_cvt_pk_bf16_f32 v10, v10, v14
	v_add_f32_e32 v14, v15, v75
	v_mul_f32_e32 v14, 0xbfb8aa3b, v14
	v_exp_f32_e32 v14, v14
	v_and_b32_e32 v21, 0xffff0000, v155
	v_add_f32_e32 v14, 1.0, v14
	v_rcp_f32_e32 v14, v14
	s_nop 0
	v_mul_f32_e64 v14, v14, -v67
	v_add_f32_e32 v15, v14, v14
	v_exp_f32_e32 v15, v15
	s_nop 0
	v_sub_f32_e32 v15, 1.0, v15
	v_max_f32_e32 v15, 0, v15
	v_sqrt_f32_e32 v15, v15
	s_nop 0
	v_mul_f32_e32 v11, v11, v15
	v_mul_f32_e32 v11, v11, v19
	v_cvt_pk_bf16_f32 v11, v11, v14
	v_add_f32_e32 v14, v16, v76
	v_mul_f32_e32 v14, 0xbfb8aa3b, v14
	v_exp_f32_e32 v14, v14
	s_nop 0
	v_add_f32_e32 v14, 1.0, v14
	v_rcp_f32_e32 v14, v14
	s_nop 0
	v_mul_f32_e64 v14, v14, -v68
	v_add_f32_e32 v15, v14, v14
	v_exp_f32_e32 v15, v15
	s_nop 0
	v_sub_f32_e32 v15, 1.0, v15
	v_max_f32_e32 v15, 0, v15
	v_sqrt_f32_e32 v15, v15
	s_nop 0
	v_mul_f32_e32 v12, v12, v15
	v_mul_f32_e32 v12, v12, v20
	v_cvt_pk_bf16_f32 v12, v12, v14
	v_add_f32_e32 v14, v17, v77
	v_mul_f32_e32 v14, 0xbfb8aa3b, v14
	v_exp_f32_e32 v14, v14
	s_nop 0
	v_add_f32_e32 v14, 1.0, v14
	v_rcp_f32_e32 v14, v14
	s_nop 0
	v_mul_f32_e64 v14, v14, -v69
	v_add_f32_e32 v15, v14, v14
	v_exp_f32_e32 v15, v15
	s_nop 0
	v_sub_f32_e32 v15, 1.0, v15
	v_max_f32_e32 v15, 0, v15
	v_sqrt_f32_e32 v15, v15
	s_nop 0
	v_mul_f32_e32 v13, v13, v15
	v_mul_f32_e32 v13, v13, v21
	v_cvt_pk_bf16_f32 v13, v13, v14
	v_add_f32_e32 v14, v6, v6
	v_exp_f32_e32 v14, v14
	flat_store_dwordx4 v[78:79], v[10:13] offset:64
	v_sub_f32_e32 v14, 1.0, v14
	v_max_f32_e32 v14, 0, v14
	v_sqrt_f32_e32 v14, v14
	v_lshlrev_b32_e32 v10, 16, v152
	v_and_b32_e32 v11, 0xffff0000, v152
	v_lshlrev_b32_e32 v12, 16, v153
	v_mul_f32_e32 v2, v2, v14
	v_mul_f32_e32 v2, v2, v10
	v_cvt_pk_bf16_f32 v2, v2, v6
	v_add_f32_e32 v6, v7, v75
	v_mul_f32_e32 v6, 0xbfb8aa3b, v6
	v_exp_f32_e32 v6, v6
	v_and_b32_e32 v13, 0xffff0000, v153
	v_add_f32_e32 v6, 1.0, v6
	v_rcp_f32_e32 v6, v6
	s_nop 0
	v_mul_f32_e64 v6, v6, -v67
	v_add_f32_e32 v7, v6, v6
	v_exp_f32_e32 v7, v7
	s_nop 0
	v_sub_f32_e32 v7, 1.0, v7
	v_max_f32_e32 v7, 0, v7
	v_sqrt_f32_e32 v7, v7
	s_nop 0
	v_mul_f32_e32 v3, v3, v7
	v_mul_f32_e32 v3, v3, v11
	v_cvt_pk_bf16_f32 v3, v3, v6
	v_add_f32_e32 v6, v8, v76
	v_mul_f32_e32 v6, 0xbfb8aa3b, v6
	v_exp_f32_e32 v6, v6
	s_nop 0
	v_add_f32_e32 v6, 1.0, v6
	v_rcp_f32_e32 v6, v6
	s_nop 0
	v_mul_f32_e64 v6, v6, -v68
	v_add_f32_e32 v7, v6, v6
	v_exp_f32_e32 v7, v7
	s_nop 0
	v_sub_f32_e32 v7, 1.0, v7
	v_max_f32_e32 v7, 0, v7
	v_sqrt_f32_e32 v7, v7
	s_nop 0
	v_mul_f32_e32 v4, v4, v7
	v_mul_f32_e32 v4, v4, v12
	v_cvt_pk_bf16_f32 v4, v4, v6
	v_add_f32_e32 v6, v9, v77
	v_mul_f32_e32 v6, 0xbfb8aa3b, v6
	v_exp_f32_e32 v6, v6
	s_nop 0
	v_add_f32_e32 v6, 1.0, v6
	v_rcp_f32_e32 v6, v6
	s_nop 0
	v_mul_f32_e64 v6, v6, -v69
	v_add_f32_e32 v7, v6, v6
	v_exp_f32_e32 v7, v7
	s_nop 0
	v_sub_f32_e32 v7, 1.0, v7
	v_max_f32_e32 v7, 0, v7
	v_sqrt_f32_e32 v7, v7
	s_nop 0
	v_mul_f32_e32 v5, v5, v7
	v_mul_f32_e32 v5, v5, v13
	v_cvt_pk_bf16_f32 v5, v5, v6
	flat_store_dwordx4 v[80:81], v[2:5] offset:64
	s_cbranch_vccnz .LBB0_451
	s_andn2_b64 vcc, exec, s[28:29]
	s_cbranch_vccnz .LBB0_450
	s_barrier
	s_branch .LBB0_450

.LBB0_1126:
	v_readlane_b32 s10, v254, 0
	s_cmp_le_i32 s10, s0
	s_cselect_b64 s[0:1], -1, 0
	s_and_b64 s[18:19], s[0:1], s[18:19]
	s_andn2_b64 vcc, exec, s[18:19]
	v_readlane_b32 s11, v254, 1
	s_cbranch_vccnz .LBB0_1144
	v_readlane_b32 s12, v254, 2
	v_readlane_b32 s13, v254, 3
	v_readlane_b32 s14, v254, 4
	v_readlane_b32 s15, v254, 5
	s_mov_b64 s[26:27], s[14:15]
	s_mov_b32 s28, s2
	s_mov_b64 s[0:1], s[12:13]
	v_mov_b32_e32 v23, v0
	s_mov_b32 s34, 14
	v_readfirstlane_b32 s0, v23
	s_mov_b32 s30, 15
	s_cmpk_lt_i32 s28, 0x80
	s_cbranch_scc0 .LBB0_1144
	s_ashr_i32 s35, s34, 31
	s_ashr_i32 s1, s0, 6
	s_lshl_b64 s[10:11], s[34:35], 3
	s_add_u32 s10, s94, s10
	v_readlane_b32 s12, v254, 63
	s_addc_u32 s11, s95, s11
	v_readlane_b32 s13, v255, 0
	s_ashr_i32 s31, s30, 31
	s_lshl_b32 s66, s12, 6
	s_lshl_b64 s[12:13], s[30:31], 3
	s_add_u32 s12, s94, s12
	s_addc_u32 s13, s95, s13
	s_load_dwordx2 s[10:11], s[10:11], 0x0
	s_lshl_b64 s[14:15], s[66:67], 2
	s_load_dwordx2 s[12:13], s[12:13], 0x0
	v_and_b32_e32 v22, 63, v23
	v_lshlrev_b32_e32 v166, 2, v22
	v_and_b32_e32 v26, 64, v231
	v_add_u32_e32 v6, 64, v26
	s_waitcnt lgkmcnt(0)
	s_add_u32 s12, s12, s14
	s_addc_u32 s13, s13, s15
	s_add_u32 s10, s10, s14
	s_addc_u32 s11, s11, s15
	s_waitcnt vmcnt(0)
	v_lshl_add_u64 v[2:3], s[10:11], 0, v[166:167]
	flat_load_dword v4, v[2:3]
	v_lshl_add_u64 v[2:3], s[12:13], 0, v[166:167]
	flat_load_dword v2, v[2:3]
	v_xor_b32_e32 v7, 1, v231
	v_cmp_lt_i32_e32 vcc, v7, v6
	s_ashr_i32 s30, s28, 4
	s_and_b32 s8, s28, 15
	v_cndmask_b32_e32 v7, v231, v7, vcc
	v_lshlrev_b32_e32 v7, 2, v7
	s_ashr_i32 s31, s30, 31
	s_lshl_b32 s8, s8, 2
	s_add_u32 s8, s26, s8
	v_lshlrev_b32_e32 v14, 4, v23
	s_addc_u32 s12, s27, 0
	s_lshl_b64 s[10:11], s[30:31], 19
	v_ashrrev_i32_e32 v15, 31, v14
	s_add_u32 s10, s8, s10
	s_addc_u32 s11, s12, s11
	s_mov_b32 s8, 0x500000
	v_add_u32_e32 v28, -2, v231
	s_waitcnt vmcnt(0) lgkmcnt(0)
	v_and_b32_e32 v5, 0x7fffffff, v4
	ds_bpermute_b32 v5, v7, v5
	v_and_b32_e32 v3, 0x7fffffff, v2
	ds_bpermute_b32 v3, v7, v3
	v_max_f32_e64 v2, |v2|, |v2|
	v_max_f32_e64 v4, |v4|, |v4|
	s_waitcnt lgkmcnt(1)
	v_max_f32_e32 v5, v5, v5
	v_max_f32_e32 v4, v4, v5
	s_waitcnt lgkmcnt(0)
	v_max_f32_e32 v3, v3, v3
	v_max_f32_e32 v2, v2, v3
	v_xor_b32_e32 v3, 2, v231
	v_cmp_lt_i32_e32 vcc, v3, v6
	s_nop 1
	v_cndmask_b32_e32 v3, v231, v3, vcc
	v_lshlrev_b32_e32 v3, 2, v3
	ds_bpermute_b32 v5, v3, v4
	ds_bpermute_b32 v3, v3, v2
	s_waitcnt lgkmcnt(1)
	v_max_f32_e32 v5, v5, v5
	s_waitcnt lgkmcnt(0)
	v_max_f32_e32 v3, v3, v3
	v_max_f32_e32 v2, v2, v3
	v_xor_b32_e32 v3, 4, v231
	v_cmp_lt_i32_e32 vcc, v3, v6
	v_max_f32_e32 v4, v4, v5
	s_nop 0
	v_cndmask_b32_e32 v3, v231, v3, vcc
	v_lshlrev_b32_e32 v3, 2, v3
	ds_bpermute_b32 v5, v3, v4
	ds_bpermute_b32 v3, v3, v2
	s_waitcnt lgkmcnt(1)
	v_max_f32_e32 v5, v5, v5
	s_waitcnt lgkmcnt(0)
	v_max_f32_e32 v3, v3, v3
	v_max_f32_e32 v2, v2, v3
	v_xor_b32_e32 v3, 8, v231
	v_cmp_lt_i32_e32 vcc, v3, v6
	v_max_f32_e32 v4, v4, v5
	s_nop 0
	v_cndmask_b32_e32 v3, v231, v3, vcc
	v_lshlrev_b32_e32 v3, 2, v3
	ds_bpermute_b32 v5, v3, v4
	ds_bpermute_b32 v3, v3, v2
	s_waitcnt lgkmcnt(1)
	v_max_f32_e32 v5, v5, v5
	s_waitcnt lgkmcnt(0)
	v_max_f32_e32 v3, v3, v3
	v_max_f32_e32 v2, v2, v3
	v_xor_b32_e32 v3, 16, v231
	v_cmp_lt_i32_e32 vcc, v3, v6
	v_max_f32_e32 v4, v4, v5
	s_nop 0
	v_cndmask_b32_e32 v3, v231, v3, vcc
	v_lshlrev_b32_e32 v3, 2, v3
	ds_bpermute_b32 v5, v3, v4
	ds_bpermute_b32 v3, v3, v2
	s_waitcnt lgkmcnt(1)
	v_max_f32_e32 v5, v5, v5
	s_waitcnt lgkmcnt(0)
	v_max_f32_e32 v3, v3, v3
	v_max_f32_e32 v17, v2, v3
	v_xor_b32_e32 v2, 32, v231
	v_cmp_lt_i32_e32 vcc, v2, v6
	v_max_f32_e32 v16, v4, v5
	s_nop 0
	v_cndmask_b32_e32 v2, v231, v2, vcc
	v_lshlrev_b32_e32 v2, 2, v2
	ds_bpermute_b32 v25, v2, v16
	ds_bpermute_b32 v24, v2, v17
	v_lshlrev_b64 v[2:3], 6, v[14:15]
	v_lshl_add_u64 v[2:3], s[10:11], 0, v[2:3]
	s_mov_b64 s[10:11], 0x500000
	v_lshl_add_u64 v[4:5], v[2:3], 0, s[10:11]
	v_add_co_u32_e32 v2, vcc, s8, v2
	s_nop 1
	v_addc_co_u32_e32 v3, vcc, 0, v3, vcc
	global_load_dword v2, v[2:3], off
	global_load_dword v3, v[4:5], off offset:64
	global_load_dword v234, v[4:5], off offset:128
	global_load_dword v235, v[4:5], off offset:192
	global_load_dword v236, v[4:5], off offset:256
	global_load_dword v237, v[4:5], off offset:320
	global_load_dword v238, v[4:5], off offset:384
	global_load_dword v239, v[4:5], off offset:448
	global_load_dword v240, v[4:5], off offset:512
	global_load_dword v241, v[4:5], off offset:576
	global_load_dword v242, v[4:5], off offset:640
	global_load_dword v243, v[4:5], off offset:704
	global_load_dword v244, v[4:5], off offset:768
	global_load_dword v245, v[4:5], off offset:832
	global_load_dword v27, v[4:5], off offset:896
	global_load_dword v5, v[4:5], off offset:960
	s_waitcnt vmcnt(0) lgkmcnt(0)
	v_add_f32_e32 v18, 0, v2
	v_add_f32_e32 v19, v18, v3
	v_add_f32_e32 v20, v19, v234
	v_add_f32_e32 v21, v20, v235
	v_add_f32_e32 v10, v21, v236
	v_add_f32_e32 v11, v10, v237
	v_add_f32_e32 v12, v11, v238
	v_add_f32_e32 v13, v12, v239
	v_add_f32_e32 v6, v13, v240
	v_add_f32_e32 v7, v6, v241
	v_add_f32_e32 v8, v7, v242
	v_add_f32_e32 v9, v8, v243
	v_add_f32_e32 v2, v9, v244
	v_add_f32_e32 v3, v2, v245
	v_add_f32_e32 v4, v3, v27
	v_add_u32_e32 v27, -1, v231
	v_cmp_lt_i32_e32 vcc, v27, v26
	v_add_f32_e32 v5, v4, v5
	s_nop 0
	v_cndmask_b32_e32 v27, v27, v231, vcc
	v_lshlrev_b32_e32 v27, 2, v27
	ds_bpermute_b32 v27, v27, v5
	v_cmp_eq_u32_e32 vcc, 0, v22
	s_waitcnt lgkmcnt(0)
	v_add_f32_e32 v27, v5, v27
	v_cndmask_b32_e32 v27, v27, v5, vcc
	v_cmp_lt_i32_e32 vcc, v28, v26
	s_nop 1
	v_cndmask_b32_e32 v28, v28, v231, vcc
	v_lshlrev_b32_e32 v28, 2, v28
	ds_bpermute_b32 v28, v28, v27
	v_cmp_gt_u32_e32 vcc, 2, v22
	s_waitcnt lgkmcnt(0)
	v_add_f32_e32 v28, v27, v28
	v_cndmask_b32_e32 v27, v28, v27, vcc
	v_add_u32_e32 v28, -4, v231
	v_cmp_lt_i32_e32 vcc, v28, v26
	s_nop 1
	v_cndmask_b32_e32 v28, v28, v231, vcc
	v_lshlrev_b32_e32 v28, 2, v28
	ds_bpermute_b32 v28, v28, v27
	v_cmp_gt_u32_e32 vcc, 4, v22
	s_waitcnt lgkmcnt(0)
	v_add_f32_e32 v28, v27, v28
	v_cndmask_b32_e32 v27, v28, v27, vcc
	v_add_u32_e32 v28, -8, v231
	v_cmp_lt_i32_e32 vcc, v28, v26
	s_nop 1
	v_cndmask_b32_e32 v28, v28, v231, vcc
	v_lshlrev_b32_e32 v28, 2, v28
	ds_bpermute_b32 v28, v28, v27
	v_cmp_gt_u32_e32 vcc, 8, v22
	s_waitcnt lgkmcnt(0)
	v_add_f32_e32 v28, v27, v28
	v_cndmask_b32_e32 v27, v28, v27, vcc
	v_add_u32_e32 v28, -16, v231
	v_cmp_lt_i32_e32 vcc, v28, v26
	s_nop 1
	v_cndmask_b32_e32 v28, v28, v231, vcc
	v_lshlrev_b32_e32 v28, 2, v28
	ds_bpermute_b32 v28, v28, v27
	v_cmp_gt_u32_e32 vcc, 16, v22
	s_waitcnt lgkmcnt(0)
	v_add_f32_e32 v28, v27, v28
	v_cndmask_b32_e32 v27, v28, v27, vcc
	v_subrev_u32_e32 v28, 32, v231
	v_cmp_lt_i32_e32 vcc, v28, v26
	s_nop 1
	v_cndmask_b32_e32 v26, v28, v231, vcc
	v_lshlrev_b32_e32 v26, 2, v26
	ds_bpermute_b32 v26, v26, v27
	v_cmp_eq_u32_e32 vcc, 63, v22
	s_waitcnt lgkmcnt(0)
	v_add_f32_e32 v26, v27, v26
	s_and_saveexec_b64 s[30:31], vcc
	s_lshl_b32 s8, s1, 2
	s_add_i32 s8, s8, 0
	v_mov_b32_e32 v28, s8
	ds_write_b32 v28, v26
	s_or_b64 exec, exec, s[30:31]
	v_cmp_gt_u32_e32 vcc, 32, v22
	s_cmp_lt_i32 s1, 1
	s_waitcnt lgkmcnt(0)
	v_cndmask_b32_e32 v22, v26, v27, vcc
	v_sub_f32_e32 v22, v22, v5
	s_barrier
	s_cbranch_scc1 .LBB0_1137
	s_cmp_lt_u32 s1, 8
	s_mov_b32 s8, 0
	s_cbranch_scc1 .LBB0_1134
	s_and_b32 s8, s1, 0x7ffffff8
	s_mov_b32 s1, 0
	s_mov_b32 s10, 0

.LBB0_1562:
	s_waitcnt vmcnt(0)
	global_load_dword v9, v[4:5], off
	v_cmp_gt_i32_e32 vcc, s0, v7
	v_add_u32_e32 v7, 32, v7
	v_lshl_add_u64 v[4:5], v[4:5], 0, s[10:11]
	s_waitcnt vmcnt(0) lgkmcnt(0)
	v_cndmask_b32_e32 v10, 0, v9, vcc
	v_cmp_le_i32_e32 vcc, s8, v7
	v_add_u32_e32 v8, v10, v8
	v_add_u32_e32 v6, v9, v6
	s_or_b64 s[30:31], vcc, s[30:31]
	s_andn2_b64 exec, exec, s[30:31]
	s_cbranch_execnz .LBB0_1562
	s_or_b64 exec, exec, s[30:31]
